# barrier waits + flush leftovers by waves 1-6, flush fetch by waves 1-3, P13 remap
# baseline (speedup 1.0000x reference)
; __device__ __forceinline__ void xcd_barrier_cv(const XcdBarrier& b, const CvWork& w) {
;     asm volatile("s_waitcnt vmcnt(0)" ::: "memory");
;     const unsigned g0 = w.rel[0];
;     __syncthreads();
;     if (b.wave == 0) {
;         xb_wave0(b, w.rel + 1, g0 + 1u);
;         w.rel[0] = g0 + 1u;
;     } else if (b.wave != 0) {
;         unsigned guard = 0;
;         while (w.rel[0] == g0) { if (w.rel[1] == g0 + 1u || b.wave > 4) { __builtin_amdgcn_s_sleep(1); continue; }
;             if (!cv_one(w)) __builtin_amdgcn_s_sleep(4); if (++guard > (1u << 22)) break; }
;     }
;     asm volatile("s_waitcnt lgkmcnt(0)" ::: "memory"); __builtin_amdgcn_s_barrier(); asm volatile("" ::: "memory");
; }
.LBB0_193:
	s_add_i32 s0, 0, 0x20170
	s_waitcnt vmcnt(0)
	s_waitcnt vmcnt(16)
	v_mov_b32_e32 v0, s0
	ds_read_b32 v2, v0
	s_cmp_eq_u32 s89, 0
	s_waitcnt lgkmcnt(0)
	s_barrier
	s_cbranch_scc1 .LBB0_219
	v_mov_b32_e32 v0, s0
	ds_read_b32 v0, v0
	s_waitcnt lgkmcnt(0)
	v_cmp_ne_u32_e32 vcc, v0, v2
	s_cbranch_vccnz .LBB0_218
	s_cmp_gt_i32 s89, 6
	s_cselect_b64 s[0:1], -1, 0
	s_lshl_b32 s2, s89, 3
	s_add_i32 s3, 0, 0x20174
	s_add_i32 s10, s2, 0
	v_add_u32_e32 v3, 1, v2
	s_mov_b32 s28, 0
	s_waitcnt vmcnt(15)
	v_mov_b32_e32 v4, s3
	s_add_i32 s2, s10, 0x20180
	v_mov_b32_e32 v1, 0
	s_mov_b32 s3, 0x10000
	v_mov_b32_e32 v5, 0x10001
	s_add_i32 s10, s10, 0x20184
	s_movk_i32 s11, 0x4000
	s_mov_b32 s12, 0x8000
	s_mov_b32 s13, 0xc000
	s_mov_b32 s14, 0x14000
	s_mov_b32 s15, 0x18000
	s_mov_b32 s16, 0x1c000
	s_mov_b32 s17, 0x20000
	s_mov_b32 s18, 0x24000
	s_mov_b32 s19, 0x28000
	s_mov_b32 s20, 0x2c000
	s_mov_b32 s21, 0x30000
	s_mov_b32 s22, 0x34000
	s_mov_b32 s23, 0x38000
	s_mov_b32 s24, 0x3c000
	s_mov_b32 s25, 0xc3e00000
	s_movk_i32 s26, 0x1000
	s_add_i32 s27, 0, 0x20170
	v_mov_b32_e32 v6, 0x43e00000
	s_branch .LBB0_197

; __device__ __forceinline__ void xcd_barrier_cv(const XcdBarrier& b, const CvWork& w) {
;     asm volatile("s_waitcnt vmcnt(0)" ::: "memory");
;     const unsigned g0 = w.rel[0];
;     __syncthreads();
;     if (b.wave == 0) {
;         xb_wave0(b, w.rel + 1, g0 + 1u);
;         w.rel[0] = g0 + 1u;
;     } else if (b.wave != 0) {
;         unsigned guard = 0;
;         while (w.rel[0] == g0) { if (w.rel[1] == g0 + 1u || b.wave > 4) { __builtin_amdgcn_s_sleep(1); continue; }
;             if (!cv_one(w)) __builtin_amdgcn_s_sleep(4); if (++guard > (1u << 22)) break; }
;     }
;     asm volatile("s_waitcnt lgkmcnt(0)" ::: "memory"); __builtin_amdgcn_s_barrier(); asm volatile("" ::: "memory");
; }
.LBB0_359:
	s_cmp_lt_i32 s81, 3
	s_cbranch_scc1 .LBB0_431
	s_add_i32 s0, 0, 0x20170
	s_waitcnt vmcnt(0)
	v_mov_b32_e32 v0, s0
	ds_read_b32 v2, v0
	s_cmp_eq_u32 s89, 0
	s_waitcnt vmcnt(0) lgkmcnt(0)
	s_barrier
	s_cbranch_scc1 .LBB0_386
	v_mov_b32_e32 v0, s0
	ds_read_b32 v0, v0
	s_waitcnt lgkmcnt(0)
	v_cmp_ne_u32_e32 vcc, v0, v2
	s_cbranch_vccnz .LBB0_385
	s_cmp_gt_i32 s89, 6
	s_cselect_b64 s[0:1], -1, 0
	s_lshl_b32 s2, s89, 3
	s_add_i32 s3, 0, 0x20174
	s_add_i32 s10, s2, 0
	v_add_u32_e32 v3, 1, v2
	s_mov_b32 s28, 0
	v_mov_b32_e32 v4, s3
	s_add_i32 s2, s10, 0x20180
	v_mov_b32_e32 v1, 0
	s_mov_b32 s3, 0x10000
	v_mov_b32_e32 v5, 0x10001
	s_add_i32 s10, s10, 0x20184
	s_movk_i32 s11, 0x4000
	s_mov_b32 s12, 0x8000
	s_mov_b32 s13, 0xc000
	s_mov_b32 s14, 0x14000
	s_mov_b32 s15, 0x18000
	s_mov_b32 s16, 0x1c000
	s_mov_b32 s17, 0x20000
	s_mov_b32 s18, 0x24000
	s_mov_b32 s19, 0x28000
	s_mov_b32 s20, 0x2c000
	s_mov_b32 s21, 0x30000
	s_mov_b32 s22, 0x34000
	s_mov_b32 s23, 0x38000
	s_mov_b32 s24, 0x3c000
	s_mov_b32 s25, 0xc3e00000
	s_movk_i32 s26, 0x1000
	s_add_i32 s27, 0, 0x20170
	v_mov_b32_e32 v6, 0x43e00000
	s_branch .LBB0_364

; __device__ __forceinline__ void xcd_barrier_cv(const XcdBarrier& b, const CvWork& w) {
;     asm volatile("s_waitcnt vmcnt(0)" ::: "memory");
;     const unsigned g0 = w.rel[0];
;     __syncthreads();
;     if (b.wave == 0) {
;         xb_wave0(b, w.rel + 1, g0 + 1u);
;         w.rel[0] = g0 + 1u;
;     } else if (b.wave != 0) {
;         unsigned guard = 0;
;         while (w.rel[0] == g0) { if (w.rel[1] == g0 + 1u || b.wave > 4) { __builtin_amdgcn_s_sleep(1); continue; }
;             if (!cv_one(w)) __builtin_amdgcn_s_sleep(4); if (++guard > (1u << 22)) break; }
;     }
;     asm volatile("s_waitcnt lgkmcnt(0)" ::: "memory"); __builtin_amdgcn_s_barrier(); asm volatile("" ::: "memory");
; }
.LBB0_479:
	s_cmp_gt_i32 s81, 3
	s_cbranch_scc0 .LBB0_551
	s_add_i32 s0, 0, 0x20170
	s_waitcnt vmcnt(0)
	v_mov_b32_e32 v0, s0
	ds_read_b32 v2, v0
	s_cmp_eq_u32 s89, 0
	s_waitcnt vmcnt(0) lgkmcnt(0)
	s_barrier
	s_cbranch_scc1 .LBB0_506
	v_mov_b32_e32 v0, s0
	ds_read_b32 v0, v0
	s_waitcnt lgkmcnt(0)
	v_cmp_ne_u32_e32 vcc, v0, v2
	s_cbranch_vccnz .LBB0_505
	s_cmp_gt_i32 s89, 6
	s_cselect_b64 s[0:1], -1, 0
	s_lshl_b32 s2, s89, 3
	s_add_i32 s3, 0, 0x20174
	s_add_i32 s10, s2, 0
	v_add_u32_e32 v3, 1, v2
	s_mov_b32 s28, 0
	v_mov_b32_e32 v4, s3
	s_add_i32 s2, s10, 0x20180
	v_mov_b32_e32 v1, 0
	s_mov_b32 s3, 0x10000
	v_mov_b32_e32 v5, 0x10001
	s_add_i32 s10, s10, 0x20184
	s_movk_i32 s11, 0x4000
	s_mov_b32 s12, 0x8000
	s_mov_b32 s13, 0xc000
	s_mov_b32 s14, 0x14000
	s_mov_b32 s15, 0x18000
	s_mov_b32 s16, 0x1c000
	s_mov_b32 s17, 0x20000
	s_mov_b32 s18, 0x24000
	s_mov_b32 s19, 0x28000
	s_mov_b32 s20, 0x2c000
	s_mov_b32 s21, 0x30000
	s_mov_b32 s22, 0x34000
	s_mov_b32 s23, 0x38000
	s_mov_b32 s24, 0x3c000
	s_mov_b32 s25, 0xc3e00000
	s_movk_i32 s26, 0x1000
	s_add_i32 s27, 0, 0x20170
	v_mov_b32_e32 v6, 0x43e00000
	s_branch .LBB0_484

; __device__ __forceinline__ void xcd_barrier_cv(const XcdBarrier& b, const CvWork& w) {
;     asm volatile("s_waitcnt vmcnt(0)" ::: "memory");
;     const unsigned g0 = w.rel[0];
;     __syncthreads();
;     if (b.wave == 0) {
;         xb_wave0(b, w.rel + 1, g0 + 1u);
;         w.rel[0] = g0 + 1u;
;     } else if (b.wave != 0) {
;         unsigned guard = 0;
;         while (w.rel[0] == g0) { if (w.rel[1] == g0 + 1u || b.wave > 4) { __builtin_amdgcn_s_sleep(1); continue; }
;             if (!cv_one(w)) __builtin_amdgcn_s_sleep(4); if (++guard > (1u << 22)) break; }
;     }
;     asm volatile("s_waitcnt lgkmcnt(0)" ::: "memory"); __builtin_amdgcn_s_barrier(); asm volatile("" ::: "memory");
; }
.LBB0_643:
	s_cmp_lt_i32 s81, 5
	s_cbranch_scc1 .LBB0_715
	s_add_i32 s0, 0, 0x20170
	s_waitcnt vmcnt(0)
	v_mov_b32_e32 v0, s0
	ds_read_b32 v2, v0
	s_cmp_eq_u32 s89, 0
	s_waitcnt vmcnt(0) lgkmcnt(0)
	s_barrier
	s_cbranch_scc1 .LBB0_670
	v_mov_b32_e32 v0, s0
	ds_read_b32 v0, v0
	s_waitcnt lgkmcnt(0)
	v_cmp_ne_u32_e32 vcc, v0, v2
	s_cbranch_vccnz .LBB0_669
	s_cmp_gt_i32 s89, 6
	s_cselect_b64 s[0:1], -1, 0
	s_lshl_b32 s2, s89, 3
	s_add_i32 s3, 0, 0x20174
	s_add_i32 s10, s2, 0
	v_add_u32_e32 v3, 1, v2
	s_mov_b32 s28, 0
	v_mov_b32_e32 v4, s3
	s_add_i32 s2, s10, 0x20180
	v_mov_b32_e32 v1, 0
	s_mov_b32 s3, 0x10000
	v_mov_b32_e32 v5, 0x10001
	s_add_i32 s10, s10, 0x20184
	s_movk_i32 s11, 0x4000
	s_mov_b32 s12, 0x8000
	s_mov_b32 s13, 0xc000
	s_mov_b32 s14, 0x14000
	s_mov_b32 s15, 0x18000
	s_mov_b32 s16, 0x1c000
	s_mov_b32 s17, 0x20000
	s_mov_b32 s18, 0x24000
	s_mov_b32 s19, 0x28000
	s_mov_b32 s20, 0x2c000
	s_mov_b32 s21, 0x30000
	s_mov_b32 s22, 0x34000
	s_mov_b32 s23, 0x38000
	s_mov_b32 s24, 0x3c000
	s_mov_b32 s25, 0xc3e00000
	s_movk_i32 s26, 0x1000
	s_add_i32 s27, 0, 0x20170
	v_mov_b32_e32 v6, 0x43e00000
	s_branch .LBB0_648

; __device__ __forceinline__ void xcd_barrier_cv(const XcdBarrier& b, const CvWork& w) {
;     asm volatile("s_waitcnt vmcnt(0)" ::: "memory");
;     const unsigned g0 = w.rel[0];
;     __syncthreads();
;     if (b.wave == 0) {
;         xb_wave0(b, w.rel + 1, g0 + 1u);
;         w.rel[0] = g0 + 1u;
;     } else if (b.wave != 0) {
;         unsigned guard = 0;
;         while (w.rel[0] == g0) { if (w.rel[1] == g0 + 1u || b.wave > 4) { __builtin_amdgcn_s_sleep(1); continue; }
;             if (!cv_one(w)) __builtin_amdgcn_s_sleep(4); if (++guard > (1u << 22)) break; }
;     }
;     asm volatile("s_waitcnt lgkmcnt(0)" ::: "memory"); __builtin_amdgcn_s_barrier(); asm volatile("" ::: "memory");
; }
.LBB0_896:
	s_cmp_lt_i32 s81, 6
	s_cbranch_scc1 .LBB0_968
	s_add_i32 s0, 0, 0x20170
	s_waitcnt vmcnt(0)
	v_mov_b32_e32 v0, s0
	ds_read_b32 v2, v0
	s_cmp_eq_u32 s89, 0
	s_waitcnt vmcnt(0) lgkmcnt(0)
	s_barrier
	s_cbranch_scc1 .LBB0_923
	v_mov_b32_e32 v0, s0
	ds_read_b32 v0, v0
	s_waitcnt lgkmcnt(0)
	v_cmp_ne_u32_e32 vcc, v0, v2
	s_cbranch_vccnz .LBB0_922
	s_cmp_gt_i32 s89, 6
	s_cselect_b64 s[0:1], -1, 0
	s_lshl_b32 s2, s89, 3
	s_add_i32 s3, 0, 0x20174
	s_add_i32 s10, s2, 0
	v_add_u32_e32 v3, 1, v2
	s_mov_b32 s28, 0
	v_mov_b32_e32 v4, s3
	s_add_i32 s2, s10, 0x20180
	v_mov_b32_e32 v1, 0
	s_mov_b32 s3, 0x10000
	v_mov_b32_e32 v5, 0x10001
	s_add_i32 s10, s10, 0x20184
	s_movk_i32 s11, 0x4000
	s_mov_b32 s12, 0x8000
	s_mov_b32 s13, 0xc000
	s_mov_b32 s14, 0x14000
	s_mov_b32 s15, 0x18000
	s_mov_b32 s16, 0x1c000
	s_mov_b32 s17, 0x20000
	s_mov_b32 s18, 0x24000
	s_mov_b32 s19, 0x28000
	s_mov_b32 s20, 0x2c000
	s_mov_b32 s21, 0x30000
	s_mov_b32 s22, 0x34000
	s_mov_b32 s23, 0x38000
	s_mov_b32 s24, 0x3c000
	s_mov_b32 s25, 0xc3e00000
	s_movk_i32 s26, 0x1000
	s_add_i32 s27, 0, 0x20170
	v_mov_b32_e32 v6, 0x43e00000
	s_branch .LBB0_901

; __device__ __forceinline__ void xcd_barrier_cv(const XcdBarrier& b, const CvWork& w) {
;     asm volatile("s_waitcnt vmcnt(0)" ::: "memory");
;     const unsigned g0 = w.rel[0];
;     __syncthreads();
;     if (b.wave == 0) {
;         xb_wave0(b, w.rel + 1, g0 + 1u);
;         w.rel[0] = g0 + 1u;
;     } else if (b.wave != 0) {
;         unsigned guard = 0;
;         while (w.rel[0] == g0) { if (w.rel[1] == g0 + 1u || b.wave > 4) { __builtin_amdgcn_s_sleep(1); continue; }
;             if (!cv_one(w)) __builtin_amdgcn_s_sleep(4); if (++guard > (1u << 22)) break; }
;     }
;     asm volatile("s_waitcnt lgkmcnt(0)" ::: "memory"); __builtin_amdgcn_s_barrier(); asm volatile("" ::: "memory");
; }
.LBB0_972:
	s_cmp_lt_u32 s81, 7
	s_cbranch_scc1 .LBB0_1044
	s_add_i32 s0, 0, 0x20170
	s_waitcnt vmcnt(0)
	v_mov_b32_e32 v0, s0
	ds_read_b32 v2, v0
	s_cmp_eq_u32 s89, 0
	s_waitcnt lgkmcnt(0)
	s_barrier
	s_cbranch_scc1 .LBB0_999
	v_mov_b32_e32 v0, s0
	ds_read_b32 v0, v0
	s_waitcnt lgkmcnt(0)
	v_cmp_ne_u32_e32 vcc, v0, v2
	s_cbranch_vccnz .LBB0_998
	s_cmp_gt_i32 s89, 6
	s_cselect_b64 s[0:1], -1, 0
	s_lshl_b32 s2, s89, 3
	s_add_i32 s3, 0, 0x20174
	s_add_i32 s10, s2, 0
	v_add_u32_e32 v3, 1, v2
	s_mov_b32 s28, 0
	v_mov_b32_e32 v4, s3
	s_add_i32 s2, s10, 0x20180
	v_mov_b32_e32 v1, 0
	s_mov_b32 s3, 0x10000
	v_mov_b32_e32 v5, 0x10001
	s_add_i32 s10, s10, 0x20184
	s_movk_i32 s11, 0x4000
	s_mov_b32 s12, 0x8000
	s_mov_b32 s13, 0xc000
	s_mov_b32 s14, 0x14000
	s_mov_b32 s15, 0x18000
	s_mov_b32 s16, 0x1c000
	s_mov_b32 s17, 0x20000
	s_mov_b32 s18, 0x24000
	s_mov_b32 s19, 0x28000
	s_mov_b32 s20, 0x2c000
	s_mov_b32 s21, 0x30000
	s_mov_b32 s22, 0x34000
	s_mov_b32 s23, 0x38000
	s_mov_b32 s24, 0x3c000
	s_mov_b32 s25, 0xc3e00000
	s_movk_i32 s26, 0x1000
	s_add_i32 s27, 0, 0x20170
	v_mov_b32_e32 v6, 0x43e00000
	s_branch .LBB0_977

; __device__ __forceinline__ void xcd_barrier_cv(const XcdBarrier& b, const CvWork& w) {
;     asm volatile("s_waitcnt vmcnt(0)" ::: "memory");
;     const unsigned g0 = w.rel[0];
;     __syncthreads();
;     if (b.wave == 0) {
;         xb_wave0(b, w.rel + 1, g0 + 1u);
;         w.rel[0] = g0 + 1u;
;     } else if (b.wave != 0) {
;         unsigned guard = 0;
;         while (w.rel[0] == g0) { if (w.rel[1] == g0 + 1u || b.wave > 4) { __builtin_amdgcn_s_sleep(1); continue; }
;             if (!cv_one(w)) __builtin_amdgcn_s_sleep(4); if (++guard > (1u << 22)) break; }
;     }
;     asm volatile("s_waitcnt lgkmcnt(0)" ::: "memory"); __builtin_amdgcn_s_barrier(); asm volatile("" ::: "memory");
; }
.LBB0_1090:
	s_add_i32 s0, 0, 0x20170
	s_waitcnt vmcnt(0)
	v_mov_b32_e32 v0, s0
	ds_read_b32 v2, v0
	s_cmp_eq_u32 s89, 0
	s_waitcnt lgkmcnt(0)
	s_barrier
	s_cbranch_scc1 .LBB0_1116
	v_mov_b32_e32 v0, s0
	ds_read_b32 v0, v0
	s_waitcnt lgkmcnt(0)
	v_cmp_ne_u32_e32 vcc, v0, v2
	s_cbranch_vccnz .LBB0_1115
	s_cmp_gt_i32 s89, 6
	s_cselect_b64 s[0:1], -1, 0
	s_lshl_b32 s2, s89, 3
	s_add_i32 s3, 0, 0x20174
	s_add_i32 s10, s2, 0
	v_add_u32_e32 v3, 1, v2
	s_mov_b32 s28, 0
	v_mov_b32_e32 v4, s3
	s_add_i32 s2, s10, 0x20180
	v_mov_b32_e32 v1, 0
	s_mov_b32 s3, 0x10000
	v_mov_b32_e32 v5, 0x10001
	s_add_i32 s10, s10, 0x20184
	s_movk_i32 s11, 0x4000
	s_mov_b32 s12, 0x8000
	s_mov_b32 s13, 0xc000
	s_mov_b32 s14, 0x14000
	s_mov_b32 s15, 0x18000
	s_mov_b32 s16, 0x1c000
	s_mov_b32 s17, 0x20000
	s_mov_b32 s18, 0x24000
	s_mov_b32 s19, 0x28000
	s_mov_b32 s20, 0x2c000
	s_mov_b32 s21, 0x30000
	s_mov_b32 s22, 0x34000
	s_mov_b32 s23, 0x38000
	s_mov_b32 s24, 0x3c000
	s_mov_b32 s25, 0xc3e00000
	s_movk_i32 s26, 0x1000
	s_add_i32 s27, 0, 0x20170
	v_mov_b32_e32 v6, 0x43e00000
	s_branch .LBB0_1094

; __device__ __forceinline__ void xcd_barrier_cv(const XcdBarrier& b, const CvWork& w) {
;     asm volatile("s_waitcnt vmcnt(0)" ::: "memory");
;     const unsigned g0 = w.rel[0];
;     __syncthreads();
;     if (b.wave == 0) {
;         xb_wave0(b, w.rel + 1, g0 + 1u);
;         w.rel[0] = g0 + 1u;
;     } else if (b.wave != 0) {
;         unsigned guard = 0;
;         while (w.rel[0] == g0) { if (w.rel[1] == g0 + 1u || b.wave > 4) { __builtin_amdgcn_s_sleep(1); continue; }
;             if (!cv_one(w)) __builtin_amdgcn_s_sleep(4); if (++guard > (1u << 22)) break; }
;     }
;     asm volatile("s_waitcnt lgkmcnt(0)" ::: "memory"); __builtin_amdgcn_s_barrier(); asm volatile("" ::: "memory");
; }
.LBB0_1217:
	s_cmp_lt_i32 s81, 9
	s_cbranch_scc1 .LBB0_1289
	s_add_i32 s0, 0, 0x20170
	s_waitcnt vmcnt(0)
	v_mov_b32_e32 v0, s0
	ds_read_b32 v2, v0
	s_cmp_eq_u32 s89, 0
	s_waitcnt vmcnt(0) lgkmcnt(0)
	s_barrier
	s_cbranch_scc1 .LBB0_1244
	v_mov_b32_e32 v0, s0
	ds_read_b32 v0, v0
	s_waitcnt lgkmcnt(0)
	v_cmp_ne_u32_e32 vcc, v0, v2
	s_cbranch_vccnz .LBB0_1243
	s_cmp_gt_i32 s89, 6
	s_cselect_b64 s[0:1], -1, 0
	s_lshl_b32 s2, s89, 3
	s_add_i32 s3, 0, 0x20174
	s_add_i32 s10, s2, 0
	v_add_u32_e32 v3, 1, v2
	s_mov_b32 s28, 0
	v_mov_b32_e32 v4, s3
	s_add_i32 s2, s10, 0x20180
	v_mov_b32_e32 v1, 0
	s_mov_b32 s3, 0x10000
	v_mov_b32_e32 v5, 0x10001
	s_add_i32 s10, s10, 0x20184
	s_movk_i32 s11, 0x4000
	s_mov_b32 s12, 0x8000
	s_mov_b32 s13, 0xc000
	s_mov_b32 s14, 0x14000
	s_mov_b32 s15, 0x18000
	s_mov_b32 s16, 0x1c000
	s_mov_b32 s17, 0x20000
	s_mov_b32 s18, 0x24000
	s_mov_b32 s19, 0x28000
	s_mov_b32 s20, 0x2c000
	s_mov_b32 s21, 0x30000
	s_mov_b32 s22, 0x34000
	s_mov_b32 s23, 0x38000
	s_mov_b32 s24, 0x3c000
	s_mov_b32 s25, 0xc3e00000
	s_movk_i32 s26, 0x1000
	s_add_i32 s27, 0, 0x20170
	v_mov_b32_e32 v6, 0x43e00000
	s_branch .LBB0_1222

; __device__ __forceinline__ int lane_id_now() { unsigned z = 0u; asm volatile("" : "+v"(z)); return (int)__builtin_amdgcn_mbcnt_hi(~0u, __builtin_amdgcn_mbcnt_lo(~0u, z)); }
; __device__ __forceinline__ bool cv_one(const CvWork& w) {
;     if (w.wave == 0) return false;
;     int it = __builtin_amdgcn_readfirstlane(w.cur[2 * w.wave]); const int end = __builtin_amdgcn_readfirstlane(w.cur[2 * w.wave + 1]);
;     if (it >= end) {
;         if (it > CV_ITEMS) return false;
;         unsigned base = 0u; if (lane_id_now() == 0) base = __hip_atomic_fetch_add(w.q, (unsigned)CV_BATCH, __ATOMIC_RELAXED, __HIP_MEMORY_SCOPE_AGENT);
;         base = __builtin_amdgcn_readfirstlane(base);
;         if (base >= (unsigned)CV_ITEMS) { w.cur[2 * w.wave] = CV_ITEMS + 1; w.cur[2 * w.wave + 1] = 0; return false; }
;         it = (int)base; w.cur[2 * w.wave + 1] = (int)base + CV_BATCH;
;     }
;     TItem d; { int r = it; const int e = r / CV_I_UP; r -= e * CV_I_UP; const int nb_ = 2 * FF / 32, kb = r / nb_, nbi = r % nb_;
;         d.src = w.wup + (size_t)e * D * 2 * FF + (size_t)(128 * kb) * (2 * FF) + 32 * nbi; d.dst = (bf16*)(w.wup8 + (size_t)e * 2 * FF * D + (size_t)(32 * nbi) * D + 128 * kb);
;         d.gain = w.gain + 128 * kb; d.N = 2 * FF; d.ldk = D; }
;     const int lane = lane_id_now();
;     f32x4 r[16], g[4]; titem8_load<true, true>(d, lane, r, g); titem8_store<true, true>(d, lane, r, g);
;     w.cur[2 * w.wave] = it + 1;
;     return true;
; }
; __device__ __forceinline__ void cv_flush(const CvWork& w) { while (cv_one(w)) {} }
.LBB0_1413:
	s_cmp_eq_u32 s89, 0
	s_cselect_b64 s[0:1], -1, 0
	s_and_b64 vcc, exec, s[0:1]
	s_cbranch_vccnz .LBB0_1430
	s_cmp_gt_u32 s89, 6
	s_cbranch_scc1 .LBB0_1430
	s_lshl_b32 s2, s89, 3
	s_add_i32 s3, s2, 0
	s_add_i32 s2, s3, 0x20180
	v_mov_b32_e32 v2, s2
	s_waitcnt lgkmcnt(0)
	v_mov_b32_e32 v1, 0
	s_mov_b32 s2, 0x10000
	v_mov_b32_e32 v3, 0x10001
	s_add_i32 s3, s3, 0x20184
	s_movk_i32 s12, 0x4000
	s_mov_b32 s13, 0x8000
	s_mov_b32 s14, 0xc000
	s_mov_b32 s15, 0x14000
	s_mov_b32 s16, 0x18000
	s_mov_b32 s17, 0x1c000
	s_mov_b32 s18, 0x20000
	s_mov_b32 s19, 0x24000
	s_mov_b32 s20, 0x28000
	s_mov_b32 s21, 0x2c000
	s_mov_b32 s22, 0x30000
	s_mov_b32 s23, 0x34000
	s_mov_b32 s24, 0x38000
	s_mov_b32 s25, 0x3c000
	s_mov_b32 s26, 0xc3e00000
	s_movk_i32 s27, 0x1000
	v_mov_b32_e32 v4, 0x43e00000
	s_branch .LBB0_1416
